# down-GEMM K-loop: lane staging offsets hoisted (B1 folded into SGPR bases), on top of v2
# speedup vs baseline: 1.0170x; 1.0170x over previous
; __device__ __forceinline__ int lane_id() { int l; asm volatile("v_mbcnt_lo_u32_b32 %0, -1, 0\n\tv_mbcnt_hi_u32_b32 %0, -1, %0" : "=v"(l)); return l; }
;     __device__ __forceinline__ bool next(int i, Unit& u) const { if (!SchedMoE::next_tab(i, u)) return false; u.a0 = A + (size_t)u.p0 * 256 * rowbytes; u.a1 = u.a0 + (size_t)128 * rowbytes; return true; }
;     ...
;     for (;;) {
;         const bool has_next = S.next(ui + 1, nxt);
;         if (!has_next) nxt = cur;
;         nxt.q = (ui + 1) & 1;
;         for (int t = 0; t < nt; t += 2) {
;             const bool last = (t == nt - 2);
;             { const int tz_ = wid * 64 + lane_id();
; #pragma unroll
;               for (int i = 0; i < 2; ++i) { int R, C; stage_rc(tz_ * 16 + i * 8192, R, C); const int Rb = Epi::PERM ? ((R & ~31) + perm32(R & 31)) : R;
;                   voffA[i] = (unsigned)(R * S.multA * S.pitchA + C) * 2u; voffB[i] = (unsigned)(Rb * S.multB * S.pitchB + C) * 2u; } }
;             if constexpr (GATHER) asm volatile("" : "+v"(gc0[0]), "+v"(gc0[1]), "+v"(gc1[0]), "+v"(gc1[1]));
;             if constexpr (PREF) { if (t == nt - 4) S.prefetch(nxt, lds); }
;     ...
;         for (int a = 0; a < 2; ++a)
; #pragma unroll
;             for (int b = 0; b < 2; ++b)
; #pragma unroll
;                 for (int m = 0; m < 4; ++m)
; #pragma unroll
;                     for (int n = 0; n < 2; ++n) acc[a][b][m][n] = (acc_t){0, 0, 0, 0};
.LBB0_1722:
	s_andn2_b64 vcc, exec, s[12:13]
	s_and_b32 s72, s71, 1
	s_cbranch_vccnz .LBB0_1740
	s_lshl_b32 s29, s72, 12
	s_add_i32 s74, s29, 0
	s_ashr_i32 s29, s28, 31
	s_lshl_b32 s54, s69, 8
	s_add_i32 s74, s74, 0x20000
	s_lshl_b64 s[46:47], s[28:29], 13
	s_ashr_i32 s55, s54, 31
	s_add_u32 s29, s48, 0x100
	s_addc_u32 s75, s49, 0
	s_add_u32 s76, s50, 0x100
	s_addc_u32 s77, s51, 0
	s_add_u32 s78, s52, 0x100
	v_mov_b32_e32 v0, 0
	s_addc_u32 s79, s53, 0
	s_mov_b32 s80, 0
	s_mov_b64 s[48:49], 0
	s_lshl_b64 s[50:51], s[54:55], 2
	v_mov_b32_e32 v1, v0
	v_mov_b32_e32 v2, v0
	v_mov_b32_e32 v3, v0
	v_mov_b32_e32 v4, v0
	v_mov_b32_e32 v5, v0
	v_mov_b32_e32 v6, v0
	v_mov_b32_e32 v7, v0
	v_mov_b32_e32 v8, v0
	v_mov_b32_e32 v9, v0
	v_mov_b32_e32 v10, v0
	v_mov_b32_e32 v11, v0
	v_mov_b32_e32 v12, v0
	v_mov_b32_e32 v13, v0
	v_mov_b32_e32 v14, v0
	v_mov_b32_e32 v15, v0
	v_mov_b32_e32 v16, v0
	v_mov_b32_e32 v17, v0
	v_mov_b32_e32 v18, v0
	v_mov_b32_e32 v19, v0
	v_mov_b32_e32 v20, v0
	v_mov_b32_e32 v21, v0
	v_mov_b32_e32 v22, v0
	v_mov_b32_e32 v23, v0
	v_mov_b32_e32 v24, v0
	v_mov_b32_e32 v25, v0
	v_mov_b32_e32 v26, v0
	v_mov_b32_e32 v27, v0
	v_mov_b32_e32 v28, v0
	v_mov_b32_e32 v29, v0
	v_mov_b32_e32 v30, v0
	v_mov_b32_e32 v31, v0
	v_mov_b32_e32 v64, v0
	v_mov_b32_e32 v65, v0
	v_mov_b32_e32 v66, v0
	v_mov_b32_e32 v67, v0
	v_mov_b32_e32 v68, v0
	v_mov_b32_e32 v69, v0
	v_mov_b32_e32 v70, v0
	v_mov_b32_e32 v71, v0
	v_mov_b32_e32 v72, v0
	v_mov_b32_e32 v73, v0
	v_mov_b32_e32 v74, v0
	v_mov_b32_e32 v75, v0
	v_mov_b32_e32 v76, v0
	v_mov_b32_e32 v77, v0
	v_mov_b32_e32 v78, v0
	v_mov_b32_e32 v79, v0
	v_mov_b32_e32 v80, v0
	v_mov_b32_e32 v81, v0
	v_mov_b32_e32 v82, v0
	v_mov_b32_e32 v83, v0
	v_mov_b32_e32 v84, v0
	v_mov_b32_e32 v85, v0
	v_mov_b32_e32 v86, v0
	v_mov_b32_e32 v87, v0
	v_mov_b32_e32 v88, v0
	v_mov_b32_e32 v89, v0
	v_mov_b32_e32 v90, v0
	v_mov_b32_e32 v91, v0
	v_mov_b32_e32 v92, v0
	v_mov_b32_e32 v93, v0
	v_mov_b32_e32 v94, v0
	v_mov_b32_e32 v95, v0
	v_mov_b32_e32 v32, v0
	v_mov_b32_e32 v33, v0
	v_mov_b32_e32 v34, v0
	v_mov_b32_e32 v35, v0
	v_mov_b32_e32 v36, v0
	v_mov_b32_e32 v37, v0
	v_mov_b32_e32 v38, v0
	v_mov_b32_e32 v39, v0
	v_mov_b32_e32 v40, v0
	v_mov_b32_e32 v41, v0
	v_mov_b32_e32 v42, v0
	v_mov_b32_e32 v43, v0
	v_mov_b32_e32 v44, v0
	v_mov_b32_e32 v45, v0
	v_mov_b32_e32 v46, v0
	v_mov_b32_e32 v47, v0
	v_mov_b32_e32 v48, v0
	v_mov_b32_e32 v49, v0
	v_mov_b32_e32 v50, v0
	v_mov_b32_e32 v51, v0
	v_mov_b32_e32 v52, v0
	v_mov_b32_e32 v53, v0
	v_mov_b32_e32 v54, v0
	v_mov_b32_e32 v55, v0
	v_mov_b32_e32 v56, v0
	v_mov_b32_e32 v57, v0
	v_mov_b32_e32 v58, v0
	v_mov_b32_e32 v59, v0
	v_mov_b32_e32 v60, v0
	v_mov_b32_e32 v61, v0
	v_mov_b32_e32 v62, v0
	v_mov_b32_e32 v63, v0
	v_mov_b32_e32 v96, v0
	v_mov_b32_e32 v97, v0
	v_mov_b32_e32 v98, v0
	v_mov_b32_e32 v99, v0
	v_mov_b32_e32 v100, v0
	v_mov_b32_e32 v101, v0
	v_mov_b32_e32 v102, v0
	v_mov_b32_e32 v103, v0
	v_mov_b32_e32 v104, v0
	v_mov_b32_e32 v105, v0
	v_mov_b32_e32 v106, v0
	v_mov_b32_e32 v107, v0
	v_mov_b32_e32 v108, v0
	v_mov_b32_e32 v109, v0
	v_mov_b32_e32 v110, v0
	v_mov_b32_e32 v111, v0
	v_mov_b32_e32 v112, v0
	v_mov_b32_e32 v113, v0
	v_mov_b32_e32 v114, v0
	v_mov_b32_e32 v115, v0
	v_mov_b32_e32 v116, v0
	v_mov_b32_e32 v117, v0
	v_mov_b32_e32 v118, v0
	v_mov_b32_e32 v119, v0
	v_mov_b32_e32 v120, v0
	v_mov_b32_e32 v121, v0
	v_mov_b32_e32 v122, v0
	v_mov_b32_e32 v123, v0
	v_mov_b32_e32 v124, v0
	v_mov_b32_e32 v125, v0
	v_mov_b32_e32 v126, v0
	v_mov_b32_e32 v127, v0
	v_mbcnt_lo_u32_b32 v142, -1, 0
	v_mbcnt_hi_u32_b32 v142, -1, v142
	v_mov_b32_e32 v143, s88
	v_lshrrev_b32_e32 v143, 6, v143
	v_and_b32_e32 v144, 3, v142
	v_lshlrev_b32_e32 v144, 4, v144
	v_and_b32_e32 v145, 32, v142
	v_xor_b32_e32 v144, v144, v145
	v_and_b32_e32 v145, 1, v143
	v_lshl_add_u32 v144, v145, 6, v144
	v_lshrrev_b32_e32 v145, 1, v143
	v_lshrrev_b32_e32 v148, 2, v142
	v_lshl_add_u32 v145, v145, 4, v148
	v_mov_b32_e32 v149, 0x800
	v_mad_u32_u24 v128, v145, v149, v144
	v_add_u32_e32 v130, 0x20000, v128
	v_lshrrev_b32_e32 v145, 2, v143
	v_lshlrev_b32_e32 v145, 5, v145
	v_lshrrev_b32_e32 v148, 4, v142
	v_lshl_add_u32 v145, v148, 3, v145
	v_bfe_u32 v148, v143, 1, 1
	v_lshl_add_u32 v145, v148, 2, v145
	v_bfe_u32 v148, v142, 2, 2
	v_add_u32_e32 v145, v145, v148
	v_mov_b32_e32 v149, 0x800
	v_mad_u32_u24 v132, v145, v149, v144
	v_add_u32_e32 v146, 0x20000, v132
	v_mov_b32_e32 v129, 0
	v_mov_b32_e32 v131, 0
	v_mov_b32_e32 v133, 0
	v_mov_b32_e32 v147, 0
.LBB0_1724:
	s_cmp_lg_u32 s64, s80
	s_cbranch_scc1 .LBB0_1733
	v_mbcnt_lo_u32_b32 v142, -1, 0
	v_mbcnt_hi_u32_b32 v142, -1, v142
	s_cmp_lt_i32 s85, 2
	s_cbranch_scc1 .LBB0_1730
	s_mov_b64 s[56:57], 0
	s_cmp_eq_u32 s85, 2
	s_mov_b64 s[54:55], 0
	s_cbranch_scc0 .LBB0_1728
	s_mov_b64 s[54:55], -1
	s_mov_b64 s[52:53], s[6:7]
	s_movk_i32 s58, 0x800
	s_and_b64 vcc, exec, s[56:57]
	s_cbranch_vccz .LBB0_1731
	s_branch .LBB0_1729

; __device__ __forceinline__ int lane_id() { int l; asm volatile("v_mbcnt_lo_u32_b32 %0, -1, 0\n\tv_mbcnt_hi_u32_b32 %0, -1, %0" : "=v"(l)); return l; }
; #define G_STAGE(bufoff, gbase, voff) do { _Pragma("unroll") for (int _i = 0; _i < 2; ++_i) \
;         __builtin_amdgcn_global_load_lds((const unsigned*)((const char*)(gbase) + (voff)[_i]), (LAS unsigned*)(lds + (bufoff) + ldsw + _i * 8192), 16, 0, 0); } while (0)
; #define G_LDA(dst, b, h) do { _Pragma("unroll") for (int m = 0; m < 4; ++m) G_LD8(dst[m], lds + G_SA(b, h) + aoff + m * 2048); } while (0)
; #define G_LDB(dst, b, h) do { _Pragma("unroll") for (int n = 0; n < 2; ++n) G_LD8(dst[n], lds + G_SB(b, h) + boff + n * 2048); } while (0)
; #define G_WAIT_V(n) asm volatile("s_waitcnt vmcnt(" #n ")" ::: "memory")
; #define G_BAR __builtin_amdgcn_s_barrier()
;     ...
;             { const int tz_ = wid * 64 + lane_id();
; #pragma unroll
;               for (int i = 0; i < 2; ++i) { int R, C; stage_rc(tz_ * 16 + i * 8192, R, C); const int Rb = Epi::PERM ? ((R & ~31) + perm32(R & 31)) : R;
;                   voffA[i] = (unsigned)(R * S.multA * S.pitchA + C) * 2u; voffB[i] = (unsigned)(Rb * S.multB * S.pitchB + C) * 2u; } }
;             if constexpr (GATHER) asm volatile("" : "+v"(gc0[0]), "+v"(gc0[1]), "+v"(gc1[0]), "+v"(gc1[1]));
;             if constexpr (PREF) { if (t == nt - 4) S.prefetch(nxt, lds); }
;             const char* a11 = cur.a1 + (size_t)(t + 1) * kstep;
;             const char* a02 = last ? nxt.a0 : cur.a0 + (size_t)(t + 2) * kstep; const char* a12 = last ? nxt.a1 : cur.a1 + (size_t)(t + 2) * kstep;
;             const char* b02 = last ? nxt.b0 : cur.b0 + (size_t)(t + 2) * kstep; const char* b12 = last ? nxt.b1 : cur.b1 + (size_t)(t + 2) * kstep;
;             G_LDB(B0, 0, 0); G_LDB(B1, 0, 1); G_SCHED; G_LDA(At, 0, 0); G_STAGE(G_SA(1, 1), a11, vA1);
;             if constexpr (GATHER) { if (last) { int tz = tid; asm volatile("" : "+v"(tz));
; #pragma unroll
;                 for (int i = 0; i < 2; ++i) { int R, C; stage_rc(tz * 16 + i * 8192, R, C); gc0[i] = S.row_off(nxt, R, lds) + (unsigned)C * 2u; gc1[i] = S.row_off(nxt, 128 + R, lds) + (unsigned)C * 2u; } } }
;             G_WAIT_L(0); G_BAR; G_MMA(0, 0, At, B0); G_MMA(0, 1, At, B1); G_WAIT_V(8); G_BAR; G_SCHED;
;             G_LDA(At, 0, 1); G_STAGE(G_SB(0, 0), b02, voffB); G_STAGE(G_SB(0, 1), b12, voffB); G_STAGE(G_SA(0, 0), a02, vA0);
.LBB0_1732:
	s_add_u32 s52, s52, s46
	s_addc_u32 s53, s53, s47
	s_add_u32 s52, s52, s50
	v_lshlrev_b32_e32 v142, 2, v142
	s_addc_u32 s53, s53, s51
	v_ashrrev_i32_e32 v143, 31, v142
	v_lshl_add_u64 v[142:143], v[142:143], 2, s[52:53]
	s_add_i32 m0, s74, s58
	s_nop 0
	global_load_lds_dwordx4 v[142:143], off
.LBB0_1733:
	s_add_i32 s81, s80, 2
	s_add_u32 s52, s78, s48
	s_addc_u32 s53, s79, s49
	s_add_u32 s58, s44, s48
	s_addc_u32 s59, s45, s49
	s_add_u32 s86, s58, 0x100
	v_add_u32_e32 v154, s66, v137
	v_add_u32_e32 v170, s67, v137
	s_addc_u32 s87, s59, 0
	ds_read_b128 v[142:145], v154
	ds_read_b128 v[146:149], v154 offset:1024
	ds_read_b128 v[150:153], v154 offset:2048
	ds_read_b128 v[154:157], v154 offset:3072
	ds_read_b128 v[158:161], v170
	ds_read_b128 v[162:165], v170 offset:1024
	ds_read_b128 v[166:169], v170 offset:2048
	ds_read_b128 v[170:173], v170 offset:3072
	s_add_u32 s56, s29, s48
	s_addc_u32 s57, s75, s49
	s_add_u32 s82, s76, s48
	s_addc_u32 s83, s77, s49
	s_add_i32 s90, s66, s22
	s_add_i32 m0, s23, 0xc000
	s_add_i32 s89, s23, 0xe000
	s_add_i32 s84, s90, 0x2000
	s_cmp_eq_u32 s65, s80
	s_cselect_b32 s55, s37, s53
	s_cselect_b32 s54, s36, s52
	s_cselect_b32 s57, s31, s57
	s_cselect_b32 s56, s30, s56
	s_cselect_b32 s53, s39, s87
	s_cselect_b32 s52, s38, s86
	v_lshl_add_u64 v[206:207], s[58:59], 0, v[128:129]
	v_lshl_add_u64 v[206:207], v[206:207], 0, s[10:11]
	ds_read_b128 v[174:177], v138
	ds_read_b128 v[178:181], v138 offset:1024
	ds_read_b128 v[182:185], v138 offset:2048
	ds_read_b128 v[186:189], v138 offset:3072
	ds_read_b128 v[190:193], v138 offset:4096
	ds_read_b128 v[194:197], v138 offset:5120
	ds_read_b128 v[198:201], v138 offset:6144
	ds_read_b128 v[202:205], v138 offset:7168
	global_load_lds_dwordx4 v[206:207], off
	v_lshl_add_u64 v[206:207], s[58:59], 0, v[130:131]
	v_lshl_add_u64 v[206:207], v[206:207], 0, s[10:11]
	s_mov_b32 m0, s89
	v_mov_b32_e32 v131, v129
	global_load_lds_dwordx4 v[206:207], off
	s_waitcnt lgkmcnt(0)
	s_barrier
	s_setprio 1
	s_waitcnt lgkmcnt(0)
	v_mfma_scale_f32_16x16x128_f8f6f4 v[124:127], v[142:149], v[174:181], v[124:127], v139, v139 op_sel_hi:[0,0,0]
	v_mfma_scale_f32_16x16x128_f8f6f4 v[120:123], v[150:157], v[174:181], v[120:123], v139, v139 op_sel_hi:[0,0,0]
	v_mfma_scale_f32_16x16x128_f8f6f4 v[116:119], v[142:149], v[182:189], v[116:119], v139, v139 op_sel_hi:[0,0,0]
	v_mfma_scale_f32_16x16x128_f8f6f4 v[112:115], v[150:157], v[182:189], v[112:115], v139, v139 op_sel_hi:[0,0,0]
	v_mfma_scale_f32_16x16x128_f8f6f4 v[108:111], v[142:149], v[190:197], v[108:111], v139, v139 op_sel_hi:[0,0,0]
	v_mfma_scale_f32_16x16x128_f8f6f4 v[104:107], v[150:157], v[190:197], v[104:107], v139, v139 op_sel_hi:[0,0,0]
	v_mfma_scale_f32_16x16x128_f8f6f4 v[100:103], v[142:149], v[198:205], v[100:103], v139, v139 op_sel_hi:[0,0,0]
	v_mfma_scale_f32_16x16x128_f8f6f4 v[96:99], v[150:157], v[198:205], v[96:99], v139, v139 op_sel_hi:[0,0,0]
	s_setprio 0
	s_setprio 1
	v_mfma_scale_f32_16x16x128_f8f6f4 v[206:209], v[158:165], v[174:181], v[60:63], v139, v139 op_sel_hi:[0,0,0]
	v_mfma_scale_f32_16x16x128_f8f6f4 v[174:177], v[166:173], v[174:181], v[56:59], v139, v139 op_sel_hi:[0,0,0]
	v_mfma_scale_f32_16x16x128_f8f6f4 v[178:181], v[158:165], v[182:189], v[52:55], v139, v139 op_sel_hi:[0,0,0]
	v_mfma_scale_f32_16x16x128_f8f6f4 v[182:185], v[166:173], v[182:189], v[48:51], v139, v139 op_sel_hi:[0,0,0]
	v_mfma_scale_f32_16x16x128_f8f6f4 v[186:189], v[158:165], v[190:197], v[44:47], v139, v139 op_sel_hi:[0,0,0]
	v_mfma_scale_f32_16x16x128_f8f6f4 v[190:193], v[166:173], v[190:197], v[40:43], v139, v139 op_sel_hi:[0,0,0]
	v_mfma_scale_f32_16x16x128_f8f6f4 v[194:197], v[158:165], v[198:205], v[36:39], v139, v139 op_sel_hi:[0,0,0]
	v_mfma_scale_f32_16x16x128_f8f6f4 v[198:201], v[166:173], v[198:205], v[32:35], v139, v139 op_sel_hi:[0,0,0]
	s_setprio 0
	s_waitcnt vmcnt(8)
	s_barrier
	s_mov_b32 m0, s90
	s_nop 3
	ds_read_b128 v[32:35], v138 offset:16384
	ds_read_b128 v[36:39], v138 offset:17408
	ds_read_b128 v[40:43], v138 offset:18432
	ds_read_b128 v[44:47], v138 offset:19456
	ds_read_b128 v[48:51], v138 offset:20480
	ds_read_b128 v[52:55], v138 offset:21504
	ds_read_b128 v[56:59], v138 offset:22528
	ds_read_b128 v[60:63], v138 offset:23552
	global_load_lds_dwordx4 v132, s[56:57]
	s_mov_b32 m0, s84
	s_cselect_b32 s59, s35, s83
	s_cselect_b32 s58, s34, s82
	s_add_i32 s80, s67, s22
	s_add_u32 s98, s56, 0x20000
	s_addc_u32 s99, s57, 0
	global_load_lds_dwordx4 v132, s[98:99]
	s_mov_b32 m0, s80
	v_mov_b32_e32 v133, v129
	global_load_lds_dwordx4 v132, s[58:59]
	s_add_i32 m0, s80, 0x2000
	s_add_u32 s100, s58, 0x20000
	s_addc_u32 s101, s59, 0
	global_load_lds_dwordx4 v132, s[100:101]
	s_mov_b32 m0, s23
	v_lshl_add_u64 v[246:247], s[56:57], 0, v[132:133]
	global_load_lds_dwordx4 v128, s[54:55]
	s_mov_b32 m0, s24
	v_lshl_add_u64 v[248:249], s[98:99], 0, v[132:133]
	global_load_lds_dwordx4 v130, s[54:55]
	s_waitcnt lgkmcnt(0)
	v_lshl_add_u64 v[250:251], s[100:101], 0, v[132:133]
	v_lshl_add_u64 v[252:253], s[54:55], 0, v[128:129]
	v_lshl_add_u64 v[134:135], s[54:55], 0, v[130:131]
	s_barrier
; #define G_STAGE(bufoff, gbase, voff) do { _Pragma("unroll") for (int _i = 0; _i < 2; ++_i) \
;         __builtin_amdgcn_global_load_lds((const unsigned*)((const char*)(gbase) + (voff)[_i]), (LAS unsigned*)(lds + (bufoff) + ldsw + _i * 8192), 16, 0, 0); } while (0)
; #define G_LDA(dst, b, h) do { _Pragma("unroll") for (int m = 0; m < 4; ++m) G_LD8(dst[m], lds + G_SA(b, h) + aoff + m * 2048); } while (0)
; #define G_LDB(dst, b, h) do { _Pragma("unroll") for (int n = 0; n < 2; ++n) G_LD8(dst[n], lds + G_SB(b, h) + boff + n * 2048); } while (0)
; #define G_WAIT_V(n) asm volatile("s_waitcnt vmcnt(" #n ")" ::: "memory")
; #define G_WAIT_L(n) asm volatile("s_waitcnt lgkmcnt(" #n ")" ::: "memory")
; #define G_BAR __builtin_amdgcn_s_barrier()
; #define G_SCHED __builtin_amdgcn_sched_barrier(0)
;     ...
;             G_WAIT_L(0); G_BAR; G_MMA(0, 0, At, B0); G_MMA(0, 1, At, B1); G_WAIT_V(8); G_BAR; G_SCHED;
;             G_LDA(At, 0, 1); G_STAGE(G_SB(0, 0), b02, voffB); G_STAGE(G_SB(0, 1), b12, voffB); G_STAGE(G_SA(0, 0), a02, vA0);
;             G_WAIT_L(0); G_BAR; G_MMA(1, 0, At, B0); G_MMA(1, 1, At, B1); G_WAIT_V(8); G_BAR; G_SCHED;
;             G_LDB(B0, 1, 0); G_LDB(B1, 1, 1); G_SCHED; G_LDA(At, 1, 0); G_STAGE(G_SA(0, 1), a12, vA1);
;             G_WAIT_L(0); G_BAR; G_MMA(0, 0, At, B0); G_MMA(0, 1, At, B1); G_WAIT_V(8); G_BAR; G_SCHED;
	s_setprio 1
	s_waitcnt lgkmcnt(0)
	v_mfma_scale_f32_16x16x128_f8f6f4 v[92:95], v[142:149], v[32:39], v[92:95], v139, v139 op_sel_hi:[0,0,0]
	v_mfma_scale_f32_16x16x128_f8f6f4 v[88:91], v[150:157], v[32:39], v[88:91], v139, v139 op_sel_hi:[0,0,0]
	v_mfma_scale_f32_16x16x128_f8f6f4 v[84:87], v[142:149], v[40:47], v[84:87], v139, v139 op_sel_hi:[0,0,0]
	v_mfma_scale_f32_16x16x128_f8f6f4 v[80:83], v[150:157], v[40:47], v[80:83], v139, v139 op_sel_hi:[0,0,0]
	v_mfma_scale_f32_16x16x128_f8f6f4 v[76:79], v[142:149], v[48:55], v[76:79], v139, v139 op_sel_hi:[0,0,0]
	v_mfma_scale_f32_16x16x128_f8f6f4 v[72:75], v[150:157], v[48:55], v[72:75], v139, v139 op_sel_hi:[0,0,0]
	v_mfma_scale_f32_16x16x128_f8f6f4 v[202:205], v[142:149], v[56:63], v[68:71], v139, v139 op_sel_hi:[0,0,0]
	v_mfma_scale_f32_16x16x128_f8f6f4 v[210:213], v[150:157], v[56:63], v[64:67], v139, v139 op_sel_hi:[0,0,0]
	s_setprio 0
	s_setprio 1
	v_mfma_scale_f32_16x16x128_f8f6f4 v[214:217], v[158:165], v[32:39], v[28:31], v139, v139 op_sel_hi:[0,0,0]
	v_mfma_scale_f32_16x16x128_f8f6f4 v[218:221], v[166:173], v[32:39], v[24:27], v139, v139 op_sel_hi:[0,0,0]
	v_mfma_scale_f32_16x16x128_f8f6f4 v[222:225], v[158:165], v[40:47], v[20:23], v139, v139 op_sel_hi:[0,0,0]
	v_mfma_scale_f32_16x16x128_f8f6f4 v[226:229], v[166:173], v[40:47], v[16:19], v139, v139 op_sel_hi:[0,0,0]
	v_mfma_scale_f32_16x16x128_f8f6f4 v[230:233], v[158:165], v[48:55], v[12:15], v139, v139 op_sel_hi:[0,0,0]
	v_mfma_scale_f32_16x16x128_f8f6f4 v[234:237], v[166:173], v[48:55], v[8:11], v139, v139 op_sel_hi:[0,0,0]
	v_mfma_scale_f32_16x16x128_f8f6f4 v[238:241], v[158:165], v[56:63], v[4:7], v139, v139 op_sel_hi:[0,0,0]
	v_mfma_scale_f32_16x16x128_f8f6f4 v[242:245], v[166:173], v[56:63], v[0:3], v139, v139 op_sel_hi:[0,0,0]
	s_setprio 0
	s_waitcnt vmcnt(8)
	s_barrier
	s_add_i32 s54, 0, 0x18000
	s_add_i32 s55, 0, 0x1c000
	v_add_u32_e32 v12, s54, v137
	v_add_u32_e32 v16, s55, v137
	s_nop 0
	ds_read_b128 v[0:3], v12
	ds_read_b128 v[4:7], v12 offset:1024
	ds_read_b128 v[8:11], v12 offset:2048
	ds_read_b128 v[12:15], v12 offset:3072
	ds_read_b128 v[142:145], v16
	ds_read_b128 v[146:149], v16 offset:1024
	ds_read_b128 v[150:153], v16 offset:2048
	ds_read_b128 v[154:157], v16 offset:3072
	s_mov_b32 m0, s25
	ds_read_b128 v[16:19], v138 offset:32768
	ds_read_b128 v[20:23], v138 offset:33792
	ds_read_b128 v[24:27], v138 offset:34816
	ds_read_b128 v[28:31], v138 offset:35840
	ds_read_b128 v[32:35], v138 offset:36864
	ds_read_b128 v[36:39], v138 offset:37888
	ds_read_b128 v[64:67], v138 offset:38912
	ds_read_b128 v[68:71], v138 offset:39936
	global_load_lds_dwordx4 v128, s[52:53]
	s_mov_b32 m0, s26
	s_nop 0
	global_load_lds_dwordx4 v130, s[52:53]
	s_waitcnt lgkmcnt(0)
	s_barrier
	s_setprio 1
	s_waitcnt lgkmcnt(0)
	v_mfma_scale_f32_16x16x128_f8f6f4 v[124:127], v[0:7], v[16:23], v[124:127], v139, v139 op_sel_hi:[0,0,0]
	v_mfma_scale_f32_16x16x128_f8f6f4 v[120:123], v[8:15], v[16:23], v[120:123], v139, v139 op_sel_hi:[0,0,0]
	v_mfma_scale_f32_16x16x128_f8f6f4 v[116:119], v[0:7], v[24:31], v[116:119], v139, v139 op_sel_hi:[0,0,0]
	v_mfma_scale_f32_16x16x128_f8f6f4 v[112:115], v[8:15], v[24:31], v[112:115], v139, v139 op_sel_hi:[0,0,0]
	v_mfma_scale_f32_16x16x128_f8f6f4 v[108:111], v[0:7], v[32:39], v[108:111], v139, v139 op_sel_hi:[0,0,0]
	v_mfma_scale_f32_16x16x128_f8f6f4 v[104:107], v[8:15], v[32:39], v[104:107], v139, v139 op_sel_hi:[0,0,0]
	v_mfma_scale_f32_16x16x128_f8f6f4 v[100:103], v[0:7], v[64:71], v[100:103], v139, v139 op_sel_hi:[0,0,0]
	v_mfma_scale_f32_16x16x128_f8f6f4 v[96:99], v[8:15], v[64:71], v[96:99], v139, v139 op_sel_hi:[0,0,0]
	s_setprio 0
	s_setprio 1
	v_mfma_scale_f32_16x16x128_f8f6f4 v[60:63], v[142:149], v[16:23], v[206:209], v139, v139 op_sel_hi:[0,0,0]
	v_mfma_scale_f32_16x16x128_f8f6f4 v[56:59], v[150:157], v[16:23], v[174:177], v139, v139 op_sel_hi:[0,0,0]
	v_mfma_scale_f32_16x16x128_f8f6f4 v[52:55], v[142:149], v[24:31], v[178:181], v139, v139 op_sel_hi:[0,0,0]
	v_mfma_scale_f32_16x16x128_f8f6f4 v[48:51], v[150:157], v[24:31], v[182:185], v139, v139 op_sel_hi:[0,0,0]
	v_mfma_scale_f32_16x16x128_f8f6f4 v[44:47], v[142:149], v[32:39], v[186:189], v139, v139 op_sel_hi:[0,0,0]
	v_mfma_scale_f32_16x16x128_f8f6f4 v[40:43], v[150:157], v[32:39], v[190:193], v139, v139 op_sel_hi:[0,0,0]
	v_mfma_scale_f32_16x16x128_f8f6f4 v[36:39], v[142:149], v[64:71], v[194:197], v139, v139 op_sel_hi:[0,0,0]
	v_mfma_scale_f32_16x16x128_f8f6f4 v[32:35], v[150:157], v[64:71], v[198:201], v139, v139 op_sel_hi:[0,0,0]
	s_setprio 0
	s_waitcnt vmcnt(8)
	s_barrier
; #define G_STAGE(bufoff, gbase, voff) do { _Pragma("unroll") for (int _i = 0; _i < 2; ++_i) \
;         __builtin_amdgcn_global_load_lds((const unsigned*)((const char*)(gbase) + (voff)[_i]), (LAS unsigned*)(lds + (bufoff) + ldsw + _i * 8192), 16, 0, 0); } while (0)
; #define G_LDA(dst, b, h) do { _Pragma("unroll") for (int m = 0; m < 4; ++m) G_LD8(dst[m], lds + G_SA(b, h) + aoff + m * 2048); } while (0)
; #define G_WAIT_V(n) asm volatile("s_waitcnt vmcnt(" #n ")" ::: "memory")
; #define G_WAIT_L(n) asm volatile("s_waitcnt lgkmcnt(" #n ")" ::: "memory")
; #define G_BAR __builtin_amdgcn_s_barrier()
; #define G_SCHED __builtin_amdgcn_sched_barrier(0)
;     ...
;             G_WAIT_L(0); G_BAR; G_MMA(0, 0, At, B0); G_MMA(0, 1, At, B1); G_WAIT_V(8); G_BAR; G_SCHED;
;             G_LDA(At, 1, 1); G_STAGE(G_SB(1, 0), b02 + kstep, voffB); G_STAGE(G_SB(1, 1), b12 + kstep, voffB); G_STAGE(G_SA(1, 0), a02 + kstep, vA0);
;             G_WAIT_L(0); G_BAR; G_MMA(1, 0, At, B0); G_MMA(1, 1, At, B1); G_WAIT_V(8); G_BAR; G_SCHED;
;         }
	s_add_i32 s52, s54, s22
	v_lshl_add_u64 v[24:25], v[246:247], 0, s[10:11]
	s_mov_b32 m0, s52
	ds_read_b128 v[16:19], v138 offset:49152
	ds_read_b128 v[20:23], v138 offset:50176
	ds_read_b128 v[158:161], v138 offset:51200
	ds_read_b128 v[162:165], v138 offset:52224
	ds_read_b128 v[166:169], v138 offset:53248
	ds_read_b128 v[170:173], v138 offset:54272
	ds_read_b128 v[174:177], v138 offset:55296
	ds_read_b128 v[178:181], v138 offset:56320
	global_load_lds_dwordx4 v[24:25], off
	v_lshl_add_u64 v[24:25], v[248:249], 0, s[10:11]
	s_add_i32 m0, s52, 0x2000
	s_add_i32 s52, s55, s22
	s_sub_u32 s98, s10, 0x20000
	s_subb_u32 s99, s11, 0
	global_load_lds_dwordx4 v[24:25], off
	v_lshl_add_u64 v[24:25], v[250:251], 0, s[98:99]
	s_mov_b32 m0, s52
	s_nop 0
	global_load_lds_dwordx4 v[24:25], off
	v_lshl_add_u64 v[24:25], v[250:251], 0, s[10:11]
	s_add_i32 m0, s52, 0x2000
	s_nop 0
	global_load_lds_dwordx4 v[24:25], off
	v_lshl_add_u64 v[24:25], v[252:253], 0, s[10:11]
	s_mov_b32 m0, s62
	s_nop 0
	global_load_lds_dwordx4 v[24:25], off
	v_lshl_add_u64 v[24:25], v[134:135], 0, s[10:11]
	s_mov_b32 m0, s63
	s_nop 0
	global_load_lds_dwordx4 v[24:25], off
	s_waitcnt lgkmcnt(0)
	s_barrier
	s_setprio 1
	s_waitcnt lgkmcnt(0)
	v_mfma_scale_f32_16x16x128_f8f6f4 v[92:95], v[0:7], v[16:23], v[92:95], v139, v139 op_sel_hi:[0,0,0]
	v_mfma_scale_f32_16x16x128_f8f6f4 v[88:91], v[8:15], v[16:23], v[88:91], v139, v139 op_sel_hi:[0,0,0]
	v_mfma_scale_f32_16x16x128_f8f6f4 v[84:87], v[0:7], v[158:165], v[84:87], v139, v139 op_sel_hi:[0,0,0]
	v_mfma_scale_f32_16x16x128_f8f6f4 v[80:83], v[8:15], v[158:165], v[80:83], v139, v139 op_sel_hi:[0,0,0]
	v_mfma_scale_f32_16x16x128_f8f6f4 v[76:79], v[0:7], v[166:173], v[76:79], v139, v139 op_sel_hi:[0,0,0]
	v_mfma_scale_f32_16x16x128_f8f6f4 v[72:75], v[8:15], v[166:173], v[72:75], v139, v139 op_sel_hi:[0,0,0]
	v_mfma_scale_f32_16x16x128_f8f6f4 v[68:71], v[0:7], v[174:181], v[202:205], v139, v139 op_sel_hi:[0,0,0]
	v_mfma_scale_f32_16x16x128_f8f6f4 v[64:67], v[8:15], v[174:181], v[210:213], v139, v139 op_sel_hi:[0,0,0]
	s_setprio 0
	s_setprio 1
	v_mfma_scale_f32_16x16x128_f8f6f4 v[28:31], v[142:149], v[16:23], v[214:217], v139, v139 op_sel_hi:[0,0,0]
	v_mfma_scale_f32_16x16x128_f8f6f4 v[24:27], v[150:157], v[16:23], v[218:221], v139, v139 op_sel_hi:[0,0,0]
	v_mfma_scale_f32_16x16x128_f8f6f4 v[20:23], v[142:149], v[158:165], v[222:225], v139, v139 op_sel_hi:[0,0,0]
	v_mfma_scale_f32_16x16x128_f8f6f4 v[16:19], v[150:157], v[158:165], v[226:229], v139, v139 op_sel_hi:[0,0,0]
	v_mfma_scale_f32_16x16x128_f8f6f4 v[12:15], v[142:149], v[166:173], v[230:233], v139, v139 op_sel_hi:[0,0,0]
	v_mfma_scale_f32_16x16x128_f8f6f4 v[8:11], v[150:157], v[166:173], v[234:237], v139, v139 op_sel_hi:[0,0,0]
	v_mfma_scale_f32_16x16x128_f8f6f4 v[4:7], v[142:149], v[174:181], v[238:241], v139, v139 op_sel_hi:[0,0,0]
	v_mfma_scale_f32_16x16x128_f8f6f4 v[0:3], v[150:157], v[174:181], v[242:245], v139, v139 op_sel_hi:[0,0,0]
	s_setprio 0
	s_waitcnt vmcnt(8)
	s_barrier
	s_add_u32 s48, s48, 0x100
	s_addc_u32 s49, s49, 0
	s_cmp_ge_i32 s81, s0
	s_cbranch_scc1 .LBB0_1735
	s_mov_b32 s80, s81
	s_branch .LBB0_1724
